# speedup vs baseline: 1.0131x; 1.0034x over previous
.LBB1_84:
	s_or_b64 exec, exec, s[50:51]
	v_cndmask_b32_e64 v60, 0, 1, s[72:73]
	v_cndmask_b32_e64 v61, 0, 1, s[4:5]
	v_cndmask_b32_e64 v62, 0, 2, s[6:7]
	s_waitcnt vmcnt(0)
	v_cndmask_b32_e64 v59, 0, 4, s[10:11]
	v_or_b32_e32 v60, v62, v60
	v_or_b32_e32 v40, v40, v61
	v_cndmask_b32_e64 v61, 0, 8, s[14:15]
	v_cndmask_b32_e64 v58, 0, 16, s[18:19]
	v_or3_b32 v59, v60, v59, v61
	v_or3_b32 v40, v40, v41, v45
	v_cndmask_b32_e64 v41, 0, 32, s[22:23]
	v_or3_b32 v58, v59, v58, v41
	v_or3_b32 v59, v46, v40, v47
	v_mov_b32_e32 v40, 0x80
	v_cndmask_b32_e64 v57, 0, 64, vcc
	v_cndmask_b32_e64 v40, 0, v40, s[28:29]
	v_mov_b32_e32 v44, 0x100
	v_or_b32_e32 v57, v57, v40
	v_mov_b32_e32 v40, 0x200
	v_cndmask_b32_e64 v44, 0, v44, s[30:31]
	v_cndmask_b32_e64 v40, 0, v40, s[34:35]
	v_mov_b32_e32 v43, 0x400
	v_or_b32_e32 v61, v44, v40
	v_mov_b32_e32 v40, 0x800
	v_cndmask_b32_e64 v43, 0, v43, s[36:37]
	v_cndmask_b32_e64 v40, 0, v40, s[38:39]
	v_mov_b32_e32 v39, 0x1000
	v_or_b32_e32 v63, v43, v40
	v_mov_b32_e32 v40, 0x2000
	v_cndmask_b32_e64 v39, 0, v39, s[40:41]
	v_cndmask_b32_e64 v40, 0, v40, s[42:43]
	v_mov_b32_e32 v38, 0x4000
	v_or_b32_e32 v65, v39, v40
	v_mov_b32_e32 v39, 0x8000
	s_mul_i32 s33, s2, 0x90
	v_lshlrev_b32_e32 v87, 4, v76
	v_cndmask_b32_e64 v38, 0, v38, s[46:47]
	v_cndmask_b32_e64 v39, 0, v39, s[44:45]
	v_add_u32_e32 v86, s33, v87
	v_or_b32_e32 v156, v38, v39
	v_or_b32_e32 v38, v86, v82
	v_min_i32_e32 v38, 0x1869f, v38
	v_ashrrev_i32_e32 v39, 31, v38
	v_lshrrev_b32_e32 v40, 2, v0
	v_lshlrev_b64 v[38:39], 9, v[38:39]
	v_and_b32_e32 v85, 12, v40
	v_mov_b32_e32 v88, 0
	v_lshl_add_u64 v[38:39], s[84:85], 0, v[38:39]
	v_lshlrev_b32_e32 v78, 2, v85
	v_mov_b32_e32 v79, v88
	v_lshl_add_u64 v[66:67], v[38:39], 0, v[78:79]
	v_add_u32_e32 v79, 0x241, v84
	v_lshrrev_b32_e32 v154, 17, v18
	v_or_b32_e32 v62, v50, v51
	v_cndmask_b32_e64 v50, v79, v154, s[72:73]
	v_lshrrev_b32_e32 v152, 17, v2
	v_cndmask_b32_e64 v51, v79, v152, s[4:5]
	v_lshlrev_b32_e32 v50, 2, v50
	v_mov_b32_e32 v72, 1
	v_or_b32_e32 v60, v48, v49
	v_or_b32_e32 v157, v56, v42
	global_load_dwordx4 v[46:49], v[66:67], off nt
	global_load_dwordx4 v[42:45], v[66:67], off offset:64 nt
	global_load_dwordx4 v[38:41], v[66:67], off offset:128 nt
	s_mov_b64 exec, s[72:73]
	ds_add_rtn_u32 v155, v50, v72 offset:28672
	s_mov_b64 exec, -1
	v_lshlrev_b32_e32 v50, 2, v51
	v_lshrrev_b32_e32 v150, 17, v19
	s_mov_b64 exec, s[4:5]
	ds_add_rtn_u32 v153, v50, v72 offset:28672
	s_mov_b64 exec, -1
	v_cndmask_b32_e64 v50, v79, v150, s[6:7]
	v_lshrrev_b32_e32 v148, 17, v3
	v_cndmask_b32_e64 v51, v79, v148, s[8:9]
	v_lshlrev_b32_e32 v50, 2, v50
	s_mov_b64 exec, s[6:7]
	ds_add_rtn_u32 v151, v50, v72 offset:28672
	s_mov_b64 exec, -1
	v_lshlrev_b32_e32 v50, 2, v51
	v_lshrrev_b32_e32 v146, 17, v20
	s_mov_b64 exec, s[8:9]
	ds_add_rtn_u32 v149, v50, v72 offset:28672
	s_mov_b64 exec, -1
	v_cndmask_b32_e64 v50, v79, v146, s[10:11]
	v_lshrrev_b32_e32 v144, 17, v4
	v_cndmask_b32_e64 v51, v79, v144, s[12:13]
	v_lshlrev_b32_e32 v50, 2, v50
	s_mov_b64 exec, s[10:11]
	ds_add_rtn_u32 v147, v50, v72 offset:28672
	s_mov_b64 exec, -1
	v_lshlrev_b32_e32 v50, 2, v51
	v_lshrrev_b32_e32 v142, 17, v21
	s_mov_b64 exec, s[12:13]
	ds_add_rtn_u32 v145, v50, v72 offset:28672
	s_mov_b64 exec, -1
	v_cndmask_b32_e64 v50, v79, v142, s[14:15]
	v_lshrrev_b32_e32 v140, 17, v5
	v_cndmask_b32_e64 v51, v79, v140, s[16:17]
	v_lshlrev_b32_e32 v50, 2, v50
	v_lshrrev_b32_e32 v138, 17, v22
	v_or_b32_e32 v92, v54, v55
	s_mov_b64 exec, s[14:15]
	ds_add_rtn_u32 v143, v50, v72 offset:28672
	s_mov_b64 exec, -1
	v_lshlrev_b32_e32 v50, 2, v51
	v_cndmask_b32_e64 v54, v79, v138, s[18:19]
	v_lshrrev_b32_e32 v136, 17, v6
	s_mov_b64 exec, s[16:17]
	ds_add_rtn_u32 v141, v50, v72 offset:28672
	s_mov_b64 exec, -1
	v_cndmask_b32_e64 v55, v79, v136, s[20:21]
	v_lshlrev_b32_e32 v54, 2, v54
	v_or_b32_e32 v64, v52, v53
	global_load_dwordx4 v[50:53], v[66:67], off offset:192 nt
	s_mov_b64 exec, s[18:19]
	ds_add_rtn_u32 v139, v54, v72 offset:28672
	s_mov_b64 exec, -1
	v_lshlrev_b32_e32 v54, 2, v55
	v_lshrrev_b32_e32 v134, 17, v23
	s_mov_b64 exec, s[20:21]
	ds_add_rtn_u32 v137, v54, v72 offset:28672
	s_mov_b64 exec, -1
	v_cndmask_b32_e64 v54, v79, v134, s[22:23]
	v_lshrrev_b32_e32 v131, 17, v7
	v_cndmask_b32_e64 v55, v79, v131, s[24:25]
	v_lshlrev_b32_e32 v54, 2, v54
	s_mov_b64 exec, s[22:23]
	ds_add_rtn_u32 v135, v54, v72 offset:28672
	s_mov_b64 exec, -1
	v_lshlrev_b32_e32 v54, 2, v55
	s_mov_b64 exec, s[24:25]
	ds_add_rtn_u32 v132, v54, v72 offset:28672
	s_mov_b64 exec, -1
	v_bitop3_b32 v54, v57, 64, v58 bitop3:0xc8
	v_lshrrev_b32_e32 v130, 17, v24
	v_cmp_eq_u32_e32 vcc, 0, v54
	v_bitop3_b32 v55, v60, 64, v59 bitop3:0xc8
	v_lshrrev_b32_e32 v126, 17, v8
	v_cndmask_b32_e32 v54, v130, v79, vcc
	s_andn2_b64 s[98:99], exec, vcc
	v_cmp_eq_u32_e32 vcc, 0, v55
	v_lshlrev_b32_e32 v54, 2, v54
	s_movk_i32 s31, 0x80
	v_cndmask_b32_e32 v55, v126, v79, vcc
	s_andn2_b64 s[100:101], exec, vcc
	s_mov_b64 exec, s[98:99]
	ds_add_rtn_u32 v133, v54, v72 offset:28672
	s_mov_b64 exec, -1
	v_lshlrev_b32_e32 v54, 2, v55
	s_mov_b64 exec, s[100:101]
	ds_add_rtn_u32 v127, v54, v72 offset:28672
	s_mov_b64 exec, -1
	v_bitop3_b32 v54, v57, s31, v58 bitop3:0xc8
	s_movk_i32 s70, 0x100
	v_or_b32_e32 v81, v57, v58
	v_lshrrev_b32_e32 v125, 17, v25
	v_cmp_eq_u32_e32 vcc, 0, v54
	v_bitop3_b32 v55, v60, s31, v59 bitop3:0xc8
	v_or_b32_e32 v91, v60, v59
	v_cndmask_b32_e32 v54, v125, v79, vcc
	s_andn2_b64 s[98:99], exec, vcc
	v_lshrrev_b32_e32 v121, 17, v9
	v_cmp_eq_u32_e32 vcc, 0, v55
	v_bitop3_b32 v58, v61, s70, v81 bitop3:0xc8
	v_lshlrev_b32_e32 v54, 2, v54
	v_cndmask_b32_e32 v55, v121, v79, vcc
	s_andn2_b64 s[100:101], exec, vcc
	v_bitop3_b32 v59, v62, s70, v91 bitop3:0xc8
	v_lshrrev_b32_e32 v123, 17, v26
	v_cmp_eq_u32_e32 vcc, 0, v58
	s_movk_i32 s36, 0x200
	s_mov_b64 exec, s[98:99]
	ds_add_rtn_u32 v128, v54, v72 offset:28672
	s_mov_b64 exec, -1
	v_lshlrev_b32_e32 v54, 2, v55
	v_cndmask_b32_e32 v58, v123, v79, vcc
	s_andn2_b64 s[98:99], exec, vcc
	v_lshrrev_b32_e32 v120, 17, v10
	v_cmp_eq_u32_e32 vcc, 0, v59
	s_mov_b64 exec, s[100:101]
	ds_add_rtn_u32 v122, v54, v72 offset:28672
	s_mov_b64 exec, -1
	v_bitop3_b32 v60, v61, s36, v81 bitop3:0xc8
	v_cndmask_b32_e32 v59, v120, v79, vcc
	s_andn2_b64 s[100:101], exec, vcc
	v_lshlrev_b32_e32 v58, 2, v58
	s_movk_i32 s40, 0x400
	v_or_b32_e32 v75, v61, v81
	global_load_dwordx4 v[54:57], v[66:67], off offset:256 nt
	v_bitop3_b32 v61, v62, s36, v91 bitop3:0xc8
	s_mov_b64 exec, s[98:99]
	ds_add_rtn_u32 v129, v58, v72 offset:28672
	s_mov_b64 exec, -1
	v_lshlrev_b32_e32 v58, 2, v59
	v_lshrrev_b32_e32 v112, 17, v27
	v_cmp_eq_u32_e32 vcc, 0, v60
	v_or_b32_e32 v80, v62, v91
	s_mov_b64 exec, s[100:101]
	ds_add_rtn_u32 v124, v58, v72 offset:28672
	s_mov_b64 exec, -1
	v_bitop3_b32 v58, v63, s40, v75 bitop3:0xc8
	v_cndmask_b32_e32 v60, v112, v79, vcc
	s_andn2_b64 s[98:99], exec, vcc
	v_lshrrev_b32_e32 v117, 17, v11
	v_cmp_eq_u32_e32 vcc, 0, v61
	v_bitop3_b32 v62, v64, s40, v80 bitop3:0xc8
	v_lshlrev_b32_e32 v60, 2, v60
	v_cndmask_b32_e32 v61, v117, v79, vcc
	s_andn2_b64 s[100:101], exec, vcc
	v_lshrrev_b32_e32 v114, 17, v28
	v_cmp_eq_u32_e32 vcc, 0, v58
	s_movk_i32 s30, 0x800
	s_mov_b64 exec, s[98:99]
	ds_add_rtn_u32 v119, v60, v72 offset:28672
	s_mov_b64 exec, -1
	v_lshlrev_b32_e32 v60, 2, v61
	v_cndmask_b32_e32 v58, v114, v79, vcc
	s_andn2_b64 s[98:99], exec, vcc
	v_lshrrev_b32_e32 v113, 17, v12
	v_cmp_eq_u32_e32 vcc, 0, v62
	v_bitop3_b32 v59, v63, s30, v75 bitop3:0xc8
	s_mov_b64 exec, s[100:101]
	ds_add_rtn_u32 v118, v60, v72 offset:28672
	s_mov_b64 exec, -1
	v_cndmask_b32_e32 v60, v113, v79, vcc
	s_andn2_b64 s[100:101], exec, vcc
	v_lshlrev_b32_e32 v58, 2, v58
	v_or_b32_e32 v73, v63, v75
	v_bitop3_b32 v63, v64, s30, v80 bitop3:0xc8
	s_mov_b64 exec, s[98:99]
	ds_add_rtn_u32 v116, v58, v72 offset:28672
	s_mov_b64 exec, -1
	v_lshlrev_b32_e32 v58, 2, v60
	v_lshrrev_b32_e32 v109, 17, v29
	v_cmp_eq_u32_e32 vcc, 0, v59
	s_movk_i32 s46, 0x1000
	s_mov_b64 exec, s[100:101]
	ds_add_rtn_u32 v115, v58, v72 offset:28672
	s_mov_b64 exec, -1
	v_cndmask_b32_e32 v58, v109, v79, vcc
	s_andn2_b64 s[98:99], exec, vcc
	v_lshrrev_b32_e32 v108, 17, v13
	v_cmp_eq_u32_e32 vcc, 0, v63
	v_bitop3_b32 v93, v65, s46, v73 bitop3:0xc8
	v_lshlrev_b32_e32 v58, 2, v58
	v_cndmask_b32_e32 v59, v108, v79, vcc
	s_andn2_b64 s[100:101], exec, vcc
	v_or_b32_e32 v74, v64, v80
	s_mov_b64 exec, s[98:99]
	ds_add_rtn_u32 v111, v58, v72 offset:28672
	s_mov_b64 exec, -1
	v_lshlrev_b32_e32 v58, 2, v59
	v_lshrrev_b32_e32 v106, 17, v30
	v_cmp_eq_u32_e32 vcc, 0, v93
	v_bitop3_b32 v64, v92, s46, v74 bitop3:0xc8
	s_mov_b64 exec, s[100:101]
	ds_add_rtn_u32 v110, v58, v72 offset:28672
	s_mov_b64 exec, -1
	v_cndmask_b32_e32 v58, v106, v79, vcc
	s_andn2_b64 s[98:99], exec, vcc
	s_movk_i32 s29, 0x2000
	v_lshlrev_b32_e32 v63, 2, v58
	v_lshrrev_b32_e32 v104, 17, v14
	v_cmp_eq_u32_e32 vcc, 0, v64
	v_or_b32_e32 v68, v65, v73
	v_bitop3_b32 v65, v65, s29, v73 bitop3:0xc8
	global_load_dwordx4 v[58:61], v[66:67], off offset:320 nt
	s_mov_b64 exec, s[98:99]
	ds_add_rtn_u32 v107, v63, v72 offset:28672
	s_mov_b64 exec, -1
	v_cndmask_b32_e32 v63, v104, v79, vcc
	s_andn2_b64 s[100:101], exec, vcc
	v_lshlrev_b32_e32 v63, 2, v63
	v_lshrrev_b32_e32 v102, 17, v31
	v_cmp_eq_u32_e32 vcc, 0, v65
	v_or_b32_e32 v69, v92, v74
	v_bitop3_b32 v92, v92, s29, v74 bitop3:0xc8
	s_mov_b64 exec, s[100:101]
	ds_add_rtn_u32 v105, v63, v72 offset:28672
	s_mov_b64 exec, -1
	v_cndmask_b32_e32 v63, v102, v79, vcc
	s_andn2_b64 s[98:99], exec, vcc
	s_movk_i32 s48, 0x4000
	v_lshlrev_b32_e32 v63, 2, v63
	v_lshrrev_b32_e32 v100, 17, v15
	v_cmp_eq_u32_e32 vcc, 0, v92
	v_bitop3_b32 v94, v156, s48, v68 bitop3:0xc8
	s_mov_b64 exec, s[98:99]
	ds_add_rtn_u32 v103, v63, v72 offset:28672
	s_mov_b64 exec, -1
	v_cndmask_b32_e32 v63, v100, v79, vcc
	s_andn2_b64 s[100:101], exec, vcc
	v_lshlrev_b32_e32 v63, 2, v63
	v_lshrrev_b32_e32 v98, 17, v32
	v_cmp_eq_u32_e32 vcc, 0, v94
	v_bitop3_b32 v95, v157, s48, v69 bitop3:0xc8
	s_mov_b64 exec, s[100:101]
	ds_add_rtn_u32 v101, v63, v72 offset:28672
	s_mov_b64 exec, -1
	v_cndmask_b32_e32 v63, v98, v79, vcc
	s_andn2_b64 s[98:99], exec, vcc
	s_mov_b32 s28, 0x8000
	v_lshlrev_b32_e32 v63, 2, v63
	v_lshrrev_b32_e32 v96, 17, v16
	v_cmp_eq_u32_e32 vcc, 0, v95
	v_bitop3_b32 v158, v156, s28, v68 bitop3:0xc8
	s_mov_b64 exec, s[98:99]
	ds_add_rtn_u32 v99, v63, v72 offset:28672
	s_mov_b64 exec, -1
	v_cndmask_b32_e32 v63, v96, v79, vcc
	s_andn2_b64 s[100:101], exec, vcc
	v_bitop3_b32 v62, v157, s28, v69 bitop3:0xc8
	v_lshlrev_b32_e32 v63, 2, v63
	v_lshrrev_b32_e32 v94, 17, v33
	v_cmp_eq_u32_e32 vcc, 0, v158
	s_mov_b64 exec, s[100:101]
	ds_add_rtn_u32 v97, v63, v72 offset:28672
	s_mov_b64 exec, -1
	v_lshrrev_b32_e32 v92, 17, v17
	v_cndmask_b32_e32 v63, v94, v79, vcc
	s_andn2_b64 s[98:99], exec, vcc
	v_cmp_eq_u32_e32 vcc, 0, v62
	v_lshlrev_b32_e32 v63, 2, v63
	s_mov_b64 exec, s[98:99]
	ds_add_rtn_u32 v95, v63, v72 offset:28672
	s_mov_b64 exec, -1
	v_cndmask_b32_e32 v62, v92, v79, vcc
	s_andn2_b64 s[100:101], exec, vcc
	v_lshlrev_b32_e32 v62, 2, v62
	s_mov_b64 exec, s[100:101]
	ds_add_rtn_u32 v93, v62, v72 offset:28672
	s_mov_b64 exec, -1
	global_load_dwordx4 v[62:65], v[66:67], off offset:384 nt
	v_or_b32_e32 v79, v156, v68
	v_or_b32_e32 v156, v157, v69
	v_and_b32_e32 v157, 64, v81
	v_and_b32_e32 v81, 0x80, v81
	v_cmp_ne_u32_e64 s[64:65], 0, v81
	v_and_b32_e32 v81, 0x80, v91
	v_cmp_ne_u32_e64 s[62:63], 0, v81
	v_and_b32_e32 v81, 0x100, v75
	v_and_b32_e32 v75, 0x200, v75
	v_cmp_ne_u32_e64 s[56:57], 0, v75
	v_and_b32_e32 v75, 0x200, v80
	v_cmp_ne_u32_e64 s[54:55], 0, v75
	v_and_b32_e32 v75, 0x400, v73
	v_and_b32_e32 v73, 0x800, v73
	v_cmp_ne_u32_e64 s[68:69], 0, v157
	v_and_b32_e32 v157, 64, v91
	v_cmp_ne_u32_e64 s[48:49], 0, v73
	v_and_b32_e32 v73, 0x800, v74
	s_waitcnt lgkmcnt(0)
	s_barrier
	ds_read_b32 v91, v88 offset:31236
	v_cmp_ne_u32_e64 s[46:47], 0, v73
	v_and_b32_e32 v73, 0x1000, v68
	v_and_b32_e32 v68, 0x2000, v68
	v_cmp_ne_u32_e64 s[40:41], 0, v68
	v_and_b32_e32 v68, 0x2000, v69
	v_cmp_ne_u32_e64 s[38:39], 0, v68
	v_and_b32_e32 v68, 0x4000, v79
	v_cmp_ne_u32_e64 s[36:37], 0, v68
	v_and_b32_e32 v68, 0x4000, v156
	s_add_i32 s92, s33, 64
	v_cmp_ne_u32_e64 s[34:35], 0, v68
	v_and_b32_e32 v68, 0x8000, v79
	s_waitcnt lgkmcnt(0)
	v_readfirstlane_b32 s71, v91
	v_cmp_ne_u32_e64 s[60:61], 0, v81
	v_and_b32_e32 v81, 0x100, v80
	v_cmp_ne_u32_e64 s[52:53], 0, v75
	v_and_b32_e32 v75, 0x400, v74
	v_cmp_ne_u32_e64 s[44:45], 0, v73
	v_and_b32_e32 v73, 0x1000, v69
	v_cmp_ne_u32_e64 s[30:31], 0, v68
	v_and_b32_e32 v68, 0x8000, v156
	s_cmpk_lt_i32 s71, 0x101
	v_cmp_lt_i32_e32 vcc, s70, v91
	v_cmp_ne_u32_e64 s[66:67], 0, v157
	v_cmp_ne_u32_e64 s[58:59], 0, v81
	v_cmp_ne_u32_e64 s[50:51], 0, v75
	v_cmp_ne_u32_e64 s[42:43], 0, v73
	v_cmp_ne_u32_e64 s[28:29], 0, v68
	s_cselect_b64 s[86:87], -1, 0
	s_mov_b64 s[70:71], -1
	v_or_b32_e32 v73, s92, v82
	s_cbranch_vccz .LBB1_91
	s_mov_b64 s[70:71], 0
	s_movk_i32 s96, 0xef
	v_mov_b32_e32 v74, v83
	s_branch .LBB1_87

	.amdhsa_kernel _Z9k_binsortPKjPKiPKfPKDv4_jPiS8_PfP6__half
		.amdhsa_group_segment_fixed_size 37232
		.amdhsa_private_segment_fixed_size 0
		.amdhsa_kernarg_size 64
		.amdhsa_user_sgpr_count 2
		.amdhsa_user_sgpr_dispatch_ptr 0
		.amdhsa_user_sgpr_queue_ptr 0
		.amdhsa_user_sgpr_kernarg_segment_ptr 1
		.amdhsa_user_sgpr_dispatch_id 0
		.amdhsa_user_sgpr_kernarg_preload_length 0
		.amdhsa_user_sgpr_kernarg_preload_offset 0
		.amdhsa_user_sgpr_private_segment_size 0
		.amdhsa_uses_dynamic_stack 0
		.amdhsa_enable_private_segment 0
		.amdhsa_system_sgpr_workgroup_id_x 1
		.amdhsa_system_sgpr_workgroup_id_y 0
		.amdhsa_system_sgpr_workgroup_id_z 0
		.amdhsa_system_sgpr_workgroup_info 0
		.amdhsa_system_vgpr_workitem_id 0
		.amdhsa_next_free_vgpr 168
		.amdhsa_next_free_sgpr 102
		.amdhsa_accum_offset 168
		.amdhsa_reserve_vcc 1
		.amdhsa_float_round_mode_32 0
		.amdhsa_float_round_mode_16_64 0
		.amdhsa_float_denorm_mode_32 3
		.amdhsa_float_denorm_mode_16_64 3
		.amdhsa_dx10_clamp 1
		.amdhsa_ieee_mode 1
		.amdhsa_fp16_overflow 0
		.amdhsa_tg_split 0
		.amdhsa_exception_fp_ieee_invalid_op 0
		.amdhsa_exception_fp_denorm_src 0
		.amdhsa_exception_fp_ieee_div_zero 0
		.amdhsa_exception_fp_ieee_overflow 0
		.amdhsa_exception_fp_ieee_underflow 0
		.amdhsa_exception_fp_ieee_inexact 0
		.amdhsa_exception_int_div_zero 0
	.end_amdhsa_kernel
